# baseline (speedup 1.0000x reference)
_Z10ode_kernelPKfPKDF16_S2_PfPKi:
	v_lshrrev_b32_e32 v167, 6, v0
	s_lshr_b32 s3, s2, 3
	v_add_u32_e32 v2, s3, v167
	s_load_dwordx4 s[4:7], s[0:1], 0x0
	s_load_dwordx2 s[12:13], s[0:1], 0x10
	v_and_b32_e32 v130, 3, v2
	v_and_b32_e32 v1, 63, v0
	v_readfirstlane_b32 s3, v130
	v_lshlrev_b32_e32 v166, 4, v1
	s_lshl_b32 s11, s3, 14
	v_lshl_or_b32 v2, v130, 17, v166
	v_mov_b32_e32 v3, 0
	s_and_b32 s17, s11, 0xc000
	s_mov_b32 s9, 0
	s_waitcnt lgkmcnt(0)
	v_lshl_add_u64 v[74:75], s[6:7], 0, v[2:3]
	s_lshl_b32 s8, s17, 1
	v_lshl_add_u64 v[46:47], v[74:75], 0, s[8:9]
	s_movk_i32 s15, 0x1000
	v_add_co_u32_e32 v18, vcc, s15, v46
	s_movk_i32 s14, 0x3000
	s_nop 0
	v_addc_co_u32_e32 v19, vcc, 0, v47, vcc
	v_add_co_u32_e32 v20, vcc, s14, v46
	s_lshl_b32 s10, s2, 10
	s_nop 0
	v_addc_co_u32_e32 v21, vcc, 0, v47, vcc
	s_and_b32 s8, s10, 0x3e000
	s_movk_i32 s16, 0x7000
	v_add_co_u32_e32 v48, vcc, s16, v46
	v_lshl_or_b32 v22, v1, 7, s8
	s_add_i32 s8, s11, 0x4000
	v_addc_co_u32_e32 v49, vcc, 0, v47, vcc
	s_movk_i32 s16, 0x5000
	s_and_b32 s8, s8, 0xc000
	v_add_co_u32_e32 v50, vcc, s16, v46
	s_lshl_b32 s8, s8, 1
	global_load_dwordx4 v[34:37], v[18:19], off offset:2048
	global_load_dwordx4 v[14:17], v[20:21], off offset:2048
	global_load_dwordx4 v[6:9], v[20:21], off offset:1024
	global_load_dwordx4 v[2:5], v[18:19], off offset:1024
	global_load_dwordx4 v[42:45], v[18:19], off offset:3072
	global_load_dwordx4 v[38:41], v[20:21], off offset:3072
	v_addc_co_u32_e32 v51, vcc, 0, v47, vcc
	v_lshl_add_u64 v[72:73], v[74:75], 0, s[8:9]
	v_add_co_u32_e32 v106, vcc, s14, v72
	global_load_dwordx4 v[10:13], v[50:51], off offset:1024
	global_load_dwordx4 v[52:55], v[50:51], off offset:2048
	global_load_dwordx4 v[56:59], v[48:49], off offset:2048
	v_addc_co_u32_e32 v107, vcc, 0, v73, vcc
	v_add_co_u32_e32 v108, vcc, s15, v72
	global_load_dwordx4 v[60:63], v[50:51], off offset:3072
	global_load_dwordx4 v[64:67], v[48:49], off offset:3072
	global_load_ushort v198, v22, s[12:13]
	v_addc_co_u32_e32 v109, vcc, 0, v73, vcc
	global_load_dwordx4 v[68:71], v[108:109], off offset:2048
	global_load_dwordx4 v[78:81], v[106:107], off offset:2048
	global_load_dwordx4 v[82:85], v[106:107], off offset:3072
	global_load_dwordx4 v[86:89], v[108:109], off offset:3072
	s_add_i32 s8, s11, 0x6000
	s_movk_i32 s16, 0x2000
	s_and_b32 s8, s8, 0xe000
	v_add_co_u32_e32 v26, vcc, s16, v46
	s_lshl_b32 s8, s8, 1
	s_nop 0
	v_addc_co_u32_e32 v27, vcc, 0, v47, vcc
	v_lshl_add_u64 v[110:111], v[74:75], 0, s[8:9]
	v_add_co_u32_e32 v112, vcc, s14, v110
	global_load_dwordx4 a[0:3], v[46:47], off
	global_load_dwordx4 a[8:11], v[46:47], off offset:1024
	global_load_dwordx4 a[12:15], v[26:27], off offset:1024
	global_load_dwordx4 a[20:23], v[26:27], off offset:2048
	global_load_dwordx4 a[16:19], v[46:47], off offset:2048
	global_load_dwordx4 a[24:27], v[46:47], off offset:3072
	global_load_dwordx4 a[4:7], v[20:21], off offset:-4096
	global_load_dwordx4 v[22:25], v[20:21], off
	global_load_dwordx4 a[28:31], v[26:27], off offset:3072
	s_nop 0
	global_load_dwordx4 v[18:21], v[18:19], off
	v_addc_co_u32_e32 v113, vcc, 0, v111, vcc
	v_add_co_u32_e32 v114, vcc, s15, v110
	v_lshl_or_b32 v199, v167, 15, v166
	s_nop 0
	v_addc_co_u32_e32 v115, vcc, 0, v111, vcc
	global_load_dwordx4 v[26:29], v[114:115], off offset:1024
	global_load_dwordx4 v[90:93], v[114:115], off offset:2048
	global_load_dwordx4 v[30:33], v[112:113], off offset:1024
	global_load_dwordx4 v[94:97], v[112:113], off offset:2048
	global_load_dwordx4 v[98:101], v[114:115], off offset:3072
	global_load_dwordx4 v[102:105], v[112:113], off offset:3072
	s_movk_i32 s8, 0x6000
	s_load_dwordx2 s[6:7], s[0:1], 0x20
	v_lshlrev_b32_e32 v76, 1, v0
	v_and_b32_e32 v200, 7, v0
	v_and_b32_e32 v128, 64, v76
	v_and_b32_e32 v179, 15, v0
	v_bfe_u32 v201, v0, 4, 1
	v_mov_b32_e32 v196, 0x44444444
	global_load_dwordx4 a[44:47], v[48:49], off offset:-4096
	s_waitcnt vmcnt(31)
	ds_write_b128 v199, v[14:17] offset:1024
	v_add_co_u32_e32 v14, vcc, s8, v46
	s_movk_i32 s8, 0x4000
	s_nop 0
	v_addc_co_u32_e32 v15, vcc, 0, v47, vcc
	s_waitcnt vmcnt(28)
	ds_write_b128 v199, v[42:45] offset:2048
	v_add_co_u32_e32 v42, vcc, s8, v46
	ds_write_b128 v199, v[34:37]
	s_nop 0
	v_addc_co_u32_e32 v43, vcc, 0, v47, vcc
	s_waitcnt vmcnt(27)
	ds_write_b128 v199, v[38:41] offset:3072
	v_add_co_u32_e32 v44, vcc, s16, v72
	global_load_dwordx4 a[36:39], v[14:15], off offset:1024
	global_load_dwordx4 a[32:35], v[42:43], off offset:1024
	global_load_dwordx4 a[48:51], v[42:43], off offset:2048
	global_load_dwordx4 a[52:55], v[14:15], off offset:2048
	global_load_dwordx4 a[60:63], v[14:15], off offset:3072
	global_load_dwordx4 a[40:43], v[50:51], off offset:-4096
	global_load_dwordx4 v[34:37], v[50:51], off
	global_load_dwordx4 v[38:41], v[48:49], off
	s_nop 0
	global_load_dwordx4 v[14:17], v[48:49], off offset:1024
	s_waitcnt vmcnt(34)
	ds_write_b128 v199, v[52:55] offset:4096
	s_waitcnt vmcnt(33)
	ds_write_b128 v199, v[56:59] offset:5120
	v_addc_co_u32_e32 v45, vcc, 0, v73, vcc
	s_xor_b32 s8, s17, 0x8000
	global_load_dwordx4 a[68:71], v[106:107], off offset:-4096
	s_waitcnt vmcnt(33)
	ds_write_b128 v199, v[60:63] offset:6144
	s_waitcnt vmcnt(32)
	ds_write_b128 v199, v[64:67] offset:7168
	v_add_co_u32_e32 v58, vcc, s16, v110
	s_lshl_b32 s8, s8, 1
	global_load_dwordx4 a[56:59], v[42:43], off offset:3072
	global_load_dwordx4 a[64:67], v[72:73], off
	global_load_dwordx4 a[72:75], v[72:73], off offset:1024
	global_load_dwordx4 a[80:83], v[72:73], off offset:2048
	global_load_dwordx4 a[84:87], v[44:45], off offset:2048
	global_load_dwordx4 a[92:95], v[44:45], off offset:3072
	global_load_dwordx4 a[76:79], v[44:45], off offset:1024
	global_load_dwordx4 a[88:91], v[72:73], off offset:3072
	global_load_dwordx4 v[46:49], v[106:107], off
	global_load_dwordx4 v[54:57], v[106:107], off offset:1024
	s_nop 0
	global_load_dwordx4 v[42:45], v[108:109], off
	global_load_dwordx4 v[50:53], v[108:109], off offset:1024
	s_waitcnt vmcnt(42)
	ds_write_b128 v199, v[68:71] offset:8192
	s_waitcnt vmcnt(41)
	ds_write_b128 v199, v[78:81] offset:9216
	s_waitcnt vmcnt(39)
	ds_write_b128 v199, v[86:89] offset:10240
	ds_write_b128 v199, v[82:85] offset:11264
	v_addc_co_u32_e32 v59, vcc, 0, v111, vcc
	v_lshl_add_u64 v[78:79], v[74:75], 0, s[8:9]
	v_add_co_u32_e32 v84, vcc, s14, v78
	global_load_dwordx4 a[96:99], v[110:111], off
	global_load_dwordx4 a[104:107], v[110:111], off offset:1024
	global_load_dwordx4 a[108:111], v[58:59], off offset:1024
	global_load_dwordx4 a[116:119], v[58:59], off offset:2048
	global_load_dwordx4 a[112:115], v[110:111], off offset:2048
	global_load_dwordx4 a[120:123], v[110:111], off offset:3072
	global_load_dwordx4 a[100:103], v[112:113], off offset:-4096
	global_load_dwordx4 v[62:65], v[112:113], off
	global_load_dwordx4 a[124:127], v[58:59], off offset:3072
	s_nop 0
	global_load_dwordx4 v[58:61], v[114:115], off
	v_addc_co_u32_e32 v85, vcc, 0, v79, vcc
	v_add_co_u32_e32 v82, vcc, s15, v78
	s_add_i32 s8, s11, 0xa000
	s_nop 0
	v_addc_co_u32_e32 v83, vcc, 0, v79, vcc
	global_load_dwordx4 v[110:113], v[82:83], off offset:2048
	global_load_dwordx4 v[106:109], v[84:85], off offset:2048
	s_waitcnt vmcnt(39)
	ds_write_b128 v199, v[90:93] offset:12288
	s_waitcnt vmcnt(37)
	ds_write_b128 v199, v[94:97] offset:13312
	s_waitcnt vmcnt(36)
	ds_write_b128 v199, v[98:101] offset:14336
	s_waitcnt vmcnt(35)
	ds_write_b128 v199, v[102:105] offset:15360
	global_load_dwordx4 a[128:131], v[78:79], off
	global_load_dwordx4 a[132:135], v[84:85], off offset:-4096
	global_load_dwordx4 a[136:139], v[78:79], off offset:1024
	global_load_dwordx4 a[144:147], v[78:79], off offset:2048
	global_load_dwordx4 v[102:105], v[82:83], off offset:3072
	global_load_dwordx4 v[98:101], v[84:85], off offset:3072
	s_and_b32 s8, s8, 0xe000
	v_add_co_u32_e32 v80, vcc, s16, v78
	s_lshl_b32 s8, s8, 1
	s_nop 0
	v_addc_co_u32_e32 v81, vcc, 0, v79, vcc
	v_lshl_add_u64 v[122:123], v[74:75], 0, s[8:9]
	v_add_co_u32_e32 v124, vcc, s14, v122
	s_add_i32 s8, s11, 0xc000
	s_nop 0
	v_addc_co_u32_e32 v125, vcc, 0, v123, vcc
	v_add_co_u32_e32 v126, vcc, s15, v122
	s_and_b32 s8, s8, 0xc000
	s_nop 0
	v_addc_co_u32_e32 v127, vcc, 0, v123, vcc
	global_load_dwordx4 v[70:73], v[124:125], off offset:1024
	global_load_dwordx4 v[114:117], v[124:125], off offset:2048
	global_load_dwordx4 v[66:69], v[126:127], off offset:1024
	global_load_dwordx4 v[118:121], v[126:127], off offset:2048
	global_load_dwordx4 a[148:151], v[80:81], off offset:2048
	global_load_dwordx4 a[156:159], v[80:81], off offset:3072
	global_load_dwordx4 v[132:135], v[126:127], off offset:3072
	global_load_dwordx4 v[136:139], v[124:125], off offset:3072
	global_load_dwordx4 a[140:143], v[80:81], off offset:1024
	global_load_dwordx4 a[152:155], v[78:79], off offset:3072
	s_nop 0
	global_load_dwordx4 v[78:81], v[84:85], off
	global_load_dwordx4 v[86:89], v[84:85], off offset:1024
	s_lshl_b32 s8, s8, 1
	v_lshl_add_u64 v[164:165], v[74:75], 0, s[8:9]
	v_add_co_u32_e32 v176, vcc, s14, v164
	s_add_i32 s11, s11, 0xe000
	s_nop 0
	v_addc_co_u32_e32 v177, vcc, 0, v165, vcc
	v_add_co_u32_e32 v184, vcc, s15, v164
	s_and_b32 s8, s11, 0xe000
	s_nop 0
	v_addc_co_u32_e32 v185, vcc, 0, v165, vcc
	global_load_dwordx4 v[140:143], v[184:185], off offset:2048
	global_load_dwordx4 v[144:147], v[176:177], off offset:2048
	global_load_dwordx4 v[148:151], v[176:177], off offset:3072
	global_load_dwordx4 v[152:155], v[184:185], off offset:3072
	s_lshl_b32 s8, s8, 1
	v_lshl_add_u64 v[186:187], v[74:75], 0, s[8:9]
	v_add_co_u32_e32 v188, vcc, s14, v186
	v_and_or_b32 v74, v76, 16, v200
	s_nop 0
	v_addc_co_u32_e32 v189, vcc, 0, v187, vcc
	v_add_co_u32_e32 v190, vcc, s15, v186
	v_lshlrev_b32_e32 v129, 2, v74
	s_nop 0
	v_addc_co_u32_e32 v191, vcc, 0, v187, vcc
	global_load_dwordx4 v[94:97], v[188:189], off offset:1024
	global_load_dwordx4 v[156:159], v[188:189], off offset:2048
	global_load_dwordx4 v[90:93], v[190:191], off offset:1024
	global_load_dwordx4 v[160:163], v[190:191], off offset:2048
	global_load_dwordx4 v[172:175], v[188:189], off offset:3072
	global_load_dwordx4 v[180:183], v[190:191], off offset:3072
	s_waitcnt lgkmcnt(0)
	global_load_dword v131, v129, s[6:7]
	global_load_dwordx4 v[74:77], v[82:83], off
	s_nop 0
	global_load_dwordx4 v[82:85], v[82:83], off offset:1024
	s_waitcnt vmcnt(32)
	ds_write_b128 v199, v[110:113] offset:16384
	s_waitcnt vmcnt(31)
	ds_write_b128 v199, v[106:109] offset:17408
	v_lshlrev_b32_e32 v106, 7, v130
	v_or3_b32 v202, v106, v128, v179
	v_lshlrev_b32_e32 v106, 9, v201
	v_or_b32_e32 v107, 32, v129
	v_or3_b32 v106, v106, s10, v202
	global_load_dword v178, v129, s[6:7] offset:128
	global_load_dword v192, v107, s[6:7] offset:128
	global_load_dword v193, v129, s[6:7] offset:32
	v_ashrrev_i32_e32 v107, 31, v106
	v_lshl_add_u64 v[128:129], v[106:107], 2, s[4:5]
	global_load_dword v171, v[128:129], off
	s_waitcnt vmcnt(30)
	ds_write_b128 v199, v[102:105] offset:18432
	s_waitcnt vmcnt(29)
	ds_write_b128 v199, v[98:101] offset:19456
	v_add_co_u32_e32 v98, vcc, s16, v122
	s_mov_b32 s14, 0x45000000
	s_nop 0
	v_addc_co_u32_e32 v99, vcc, 0, v123, vcc
	global_load_dwordx4 a[160:163], v[122:123], off
	global_load_dwordx4 a[168:171], v[122:123], off offset:1024
	global_load_dwordx4 a[172:175], v[98:99], off offset:1024
	global_load_dwordx4 a[180:183], v[98:99], off offset:2048
	global_load_dwordx4 a[176:179], v[122:123], off offset:2048
	global_load_dwordx4 a[184:187], v[122:123], off offset:3072
	global_load_dword v170, v[128:129], off offset:64
	global_load_dwordx4 a[164:167], v[124:125], off offset:-4096
	global_load_dwordx4 v[102:105], v[124:125], off
	global_load_dwordx4 a[188:191], v[98:99], off offset:3072
	s_nop 0
	global_load_dwordx4 v[98:101], v[126:127], off
	s_waitcnt vmcnt(36)
	ds_write_b128 v199, v[118:121] offset:20480
	ds_write_b128 v199, v[114:117] offset:21504
	global_load_dword v169, v[128:129], off offset:128
	v_add_co_u32_e32 v106, vcc, s16, v164
	s_waitcnt vmcnt(34)
	ds_write_b128 v199, v[132:135] offset:22528
	s_waitcnt vmcnt(33)
	ds_write_b128 v199, v[136:139] offset:23552
	v_addc_co_u32_e32 v107, vcc, 0, v165, vcc
	global_load_dwordx4 a[192:195], v[164:165], off
	global_load_dwordx4 a[196:199], v[176:177], off offset:-4096
	global_load_dwordx4 a[200:203], v[164:165], off offset:1024
	global_load_dwordx4 a[208:211], v[164:165], off offset:2048
	global_load_dwordx4 a[212:215], v[106:107], off offset:2048
	global_load_dwordx4 a[220:223], v[106:107], off offset:3072
	global_load_dwordx4 a[204:207], v[106:107], off offset:1024
	global_load_dwordx4 a[216:219], v[164:165], off offset:3072
	global_load_dwordx4 v[110:113], v[176:177], off
	global_load_dwordx4 v[118:121], v[176:177], off offset:1024
	s_nop 0
	global_load_dwordx4 v[106:109], v[184:185], off
	global_load_dwordx4 v[114:117], v[184:185], off offset:1024
	global_load_dword v168, v[128:129], off offset:192
	v_add_co_u32_e32 v122, vcc, s16, v186
	v_and_b32_e32 v133, 32, v0
	s_nop 0
	v_addc_co_u32_e32 v123, vcc, 0, v187, vcc
	s_waitcnt vmcnt(41)
	ds_write_b128 v199, v[140:143] offset:24576
	s_waitcnt vmcnt(40)
	ds_write_b128 v199, v[144:147] offset:25600
	s_waitcnt vmcnt(38)
	ds_write_b128 v199, v[152:155] offset:26624
	ds_write_b128 v199, v[148:151] offset:27648
	global_load_dwordx4 a[224:227], v[186:187], off
	global_load_dwordx4 a[232:235], v[186:187], off offset:1024
	global_load_dwordx4 a[236:239], v[122:123], off offset:1024
	global_load_dwordx4 a[244:247], v[122:123], off offset:2048
	global_load_dwordx4 a[240:243], v[186:187], off offset:2048
	global_load_dwordx4 a[248:251], v[186:187], off offset:3072
	global_load_dwordx4 a[228:231], v[188:189], off offset:-4096
	global_load_dwordx4 v[126:129], v[188:189], off
	global_load_dwordx4 a[252:255], v[122:123], off offset:3072
	s_nop 0
	global_load_dwordx4 v[122:125], v[190:191], off
	v_lshlrev_b32_e32 v132, 2, v201
	v_lshl_or_b32 v130, v130, 6, v133
	v_lshrrev_b32_e32 v139, 1, v0
	v_and_b32_e32 v203, 24, v139
	s_waitcnt vmcnt(44)
	ds_write_b128 v199, v[160:163] offset:28672
	ds_write_b128 v199, v[156:159] offset:29696
	s_waitcnt vmcnt(42)
	ds_write_b128 v199, v[180:183] offset:30720
	ds_write_b128 v199, v[172:175] offset:31744
	s_waitcnt vmcnt(0) lgkmcnt(0)
	v_lshrrev_b32_e32 v222, 2, v131
	v_and_or_b32 v222, v222, 8, v132
	v_mul_u32_u24_e32 v222, 0x110, v222
	v_and_or_b32 v223, v131, 31, v130
	v_add_lshl_u32 v223, v223, v222, 1
	v_or_b32_e32 v204, 0x20000, v223
	v_lshrrev_b32_e32 v222, 2, v178
	v_and_or_b32 v222, v222, 8, v132
	v_mul_u32_u24_e32 v222, 0x110, v222
	v_and_or_b32 v223, v178, 31, v130
	v_add_lshl_u32 v223, v223, v222, 1
	v_or_b32_e32 v205, 0x20000, v223
	v_lshrrev_b32_e32 v222, 2, v193
	v_and_or_b32 v222, v222, 8, v132
	v_mul_u32_u24_e32 v222, 0x110, v222
	v_and_or_b32 v223, v193, 31, v130
	v_add_lshl_u32 v223, v223, v222, 1
	v_or_b32_e32 v206, 0x20000, v223
	v_lshrrev_b32_e32 v222, 2, v192
	v_and_or_b32 v222, v222, 8, v132
	v_mul_u32_u24_e32 v222, 0x110, v222
	v_and_or_b32 v223, v192, 31, v130
	v_add_lshl_u32 v223, v223, v222, 1
	v_or_b32_e32 v207, 0x20000, v223
	s_movk_i32 s43, 0x110
	v_mad_u32_u24 v224, v179, s43, v203
	v_mov_b32_e32 v225, 0x20000
	v_lshl_or_b32 v224, v224, 1, v225
	s_lshl_b32 s43, s3, 1
	s_add_u32 s52, s43, 0
	s_and_b32 s52, s52, 7
	s_lshl_b32 s52, s52, 6
	s_nop 0
	v_add_u32_e32 v208, s52, v224
	s_add_u32 s52, s43, 1
	s_and_b32 s52, s52, 7
	s_lshl_b32 s52, s52, 6
	s_sub_u32 s52, s52, 64
	s_nop 0
	v_add_u32_e32 v209, s52, v224
	s_add_u32 s52, s43, 2
	s_and_b32 s52, s52, 7
	s_lshl_b32 s52, s52, 6
	s_nop 0
	v_add_u32_e32 v211, s52, v224
	s_add_u32 s52, s43, 3
	s_and_b32 s52, s52, 7
	s_lshl_b32 s52, s52, 6
	s_nop 0
	v_add_u32_e32 v212, s52, v224
	s_add_u32 s52, s43, 4
	s_and_b32 s52, s52, 7
	s_lshl_b32 s52, s52, 6
	s_nop 0
	v_add_u32_e32 v213, s52, v224
	s_add_u32 s52, s43, 5
	s_and_b32 s52, s52, 7
	s_lshl_b32 s52, s52, 6
	s_nop 0
	v_add_u32_e32 v214, s52, v224
	s_add_u32 s52, s43, 6
	s_and_b32 s52, s52, 7
	s_lshl_b32 s52, s52, 6
	s_nop 0
	v_add_u32_e32 v215, s52, v224
	s_add_u32 s52, s43, 7
	s_and_b32 s52, s52, 7
	s_lshl_b32 s52, s52, 6
	s_nop 0
	v_add_u32_e32 v216, s52, v224
	v_and_b32_e32 v225, 8, v0
	v_cmp_eq_u32_e32 vcc, 0, v225
	v_mov_b32_e32 v225, 0xeeeeeeee
	s_nop 1
	v_cndmask_b32_e32 v210, v225, v196, vcc
	v_and_b32_e32 v225, 47, v0
	v_cmp_eq_u32_e64 s[4:5], 0, v225
	v_lshlrev_b32_e32 v225, 4, v167
	v_lshlrev_b32_e32 v226, 3, v201
	s_mov_b32 s52, 0x24400
	v_or3_b32 v218, v225, v226, s52
	s_load_dwordx2 s[6:7], s[0:1], 0x18
	s_lshl_b32 s11, s2, 9
	s_mov_b64 s[22:23], 0
	s_mov_b32 s29, 0
	s_mov_b32 s30, 0
	v_mov_b32_e32 v221, 0
	s_mov_b32 s40, 0x3a000000
	s_mov_b32 s41, 0x34800000
	s_mov_b32 s42, 0x45000000
	v_mov_b32_e32 v217, 0x24480
	v_mov_b64_e32 v[230:231], 0
	v_mov_b64_e32 v[232:233], 0
	v_mov_b64_e32 v[234:235], 0
	v_mov_b64_e32 v[236:237], 0
	v_mov_b64_e32 v[238:239], 0
	v_mov_b64_e32 v[240:241], 0
	v_mov_b64_e32 v[242:243], 0
	v_mov_b64_e32 v[244:245], 0
	ds_write_b128 v217, v[230:233]
	v_mov_b32_e32 v178, 0
	v_fma_mixlo_f16 v131, v178, v238, v171
	v_fma_mixlo_f16 v139, v178, v238, v170
	v_fma_mixlo_f16 v147, v178, v238, v169
	v_fma_mixlo_f16 v155, v178, v238, v168
	v_fma_f32 v130, v178, v238, v171
	v_fma_f32 v138, v178, v238, v170
	v_fma_f32 v146, v178, v238, v169
	v_fma_f32 v154, v178, v238, v168
	v_fma_mix_f32 v130, v130, 1.0, -v131 op_sel_hi:[0,0,1]
	v_fma_mix_f32 v138, v138, 1.0, -v139 op_sel_hi:[0,0,1]
	v_fma_mix_f32 v146, v146, 1.0, -v147 op_sel_hi:[0,0,1]
	v_fma_mix_f32 v154, v154, 1.0, -v155 op_sel_hi:[0,0,1]
	v_fma_mixlo_f16 v133, v130, s42, 0
	v_fma_mixlo_f16 v141, v138, s42, 0
	v_fma_mixlo_f16 v149, v146, s42, 0
	v_fma_mixlo_f16 v157, v154, s42, 0
	v_fma_mix_f32 v130, v130, s42, -v133 op_sel_hi:[0,0,1]
	v_fma_mix_f32 v138, v138, s42, -v141 op_sel_hi:[0,0,1]
	v_fma_mix_f32 v146, v146, s42, -v149 op_sel_hi:[0,0,1]
	v_fma_mix_f32 v154, v154, s42, -v157 op_sel_hi:[0,0,1]
	v_fma_mixlo_f16 v132, v130, s42, 0
	v_fma_mixlo_f16 v140, v138, s42, 0
	v_fma_mixlo_f16 v148, v146, s42, 0
	v_fma_mixlo_f16 v156, v154, s42, 0
	ds_write_b16 v204, v131
	ds_write_b16 v205, v139
	ds_write_b16 v206, v147
	ds_write_b16 v207, v155
	ds_write_b16 v204, v133 offset:544
	ds_write_b16 v205, v141 offset:544
	ds_write_b16 v206, v149 offset:544
	ds_write_b16 v207, v157 offset:544
	ds_write_b16 v204, v132 offset:1088
	ds_write_b16 v205, v140 offset:1088
	ds_write_b16 v206, v148 offset:1088
	ds_write_b16 v207, v156 offset:1088
	s_waitcnt lgkmcnt(0)
	s_barrier
	ds_read_b128 v[130:133], v208
	ds_read_b128 v[134:137], v209 offset:64
	ds_read_b128 v[138:141], v211
	ds_read_b128 v[142:145], v212
	ds_read_b128 v[146:149], v213
	ds_read_b128 v[150:153], v214
	ds_read_b128 v[154:157], v215
	ds_read_b128 v[158:161], v216
	ds_read_b128 v[180:183], v199 offset:0
	ds_read_b128 v[184:187], v199 offset:1024
	ds_read_b128 v[188:191], v199 offset:4096
	ds_read_b128 v[192:195], v199 offset:5120
	ds_read_b128 v[222:225], v199 offset:8192
	s_waitcnt lgkmcnt(6)
	ds_read_b128 v[226:229], v199 offset:9216
	v_smfmac_f32_16x16x64_f16 v[230:233], v[130:133], a[0:7], v210
	v_smfmac_f32_16x16x64_f16 v[234:237], v[130:133], v[18:25], v210
	v_smfmac_f32_16x16x64_f16 v[230:233], v[134:137], a[40:47], v210
	v_smfmac_f32_16x16x64_f16 v[234:237], v[134:137], v[34:41], v210
	v_smfmac_f32_16x16x64_f16 v[230:233], v[138:141], a[64:71], v210
	v_smfmac_f32_16x16x64_f16 v[234:237], v[138:141], v[42:49], v210
	v_smfmac_f32_16x16x64_f16 v[230:233], v[142:145], a[96:103], v210
	v_smfmac_f32_16x16x64_f16 v[234:237], v[142:145], v[58:65], v210
	v_smfmac_f32_16x16x64_f16 v[230:233], v[146:149], a[128:135], v210
	v_smfmac_f32_16x16x64_f16 v[234:237], v[146:149], v[74:81], v210
	v_smfmac_f32_16x16x64_f16 v[230:233], v[150:153], a[160:167], v210
	v_smfmac_f32_16x16x64_f16 v[234:237], v[150:153], v[98:105], v210
	v_smfmac_f32_16x16x64_f16 v[230:233], v[154:157], a[192:199], v210
	v_smfmac_f32_16x16x64_f16 v[234:237], v[154:157], v[106:113], v210
	s_waitcnt lgkmcnt(6)
	v_smfmac_f32_16x16x64_f16 v[230:233], v[158:161], a[224:231], v210
	v_smfmac_f32_16x16x64_f16 v[234:237], v[158:161], v[122:129], v210
	v_smfmac_f32_16x16x64_f16 v[238:241], v[130:133], a[16:23], v210
	s_waitcnt lgkmcnt(4)
	v_smfmac_f32_16x16x64_f16 v[242:245], v[130:133], v[180:187], v210
	ds_read_b128 v[180:183], v199 offset:12288
	ds_read_b128 v[184:187], v199 offset:13312
	v_smfmac_f32_16x16x64_f16 v[238:241], v[134:137], a[48:55], v210
	v_fmac_f32_e32 v230, s40, v231
	s_waitcnt lgkmcnt(4)
	v_smfmac_f32_16x16x64_f16 v[242:245], v[134:137], v[188:195], v210
	ds_read_b128 v[188:191], v199 offset:16384
	ds_read_b128 v[192:195], v199 offset:17408
	v_fmac_f32_e32 v234, s40, v235
	v_smfmac_f32_16x16x64_f16 v[238:241], v[138:141], a[80:87], v210
	v_fmac_f32_e32 v230, s41, v232
	s_waitcnt lgkmcnt(4)
	v_smfmac_f32_16x16x64_f16 v[242:245], v[138:141], v[222:229], v210
	ds_read_b128 v[222:225], v199 offset:20480
	ds_read_b128 v[226:229], v199 offset:21504
	v_fmac_f32_e32 v234, s41, v236
	v_smfmac_f32_16x16x64_f16 v[238:241], v[142:145], a[112:119], v210
	s_nop 0
	v_permlane32_swap_b32_e32 v230, v234
	s_waitcnt lgkmcnt(4)
	v_smfmac_f32_16x16x64_f16 v[242:245], v[142:145], v[180:187], v210
	ds_read_b128 v[180:183], v199 offset:24576
	ds_read_b128 v[184:187], v199 offset:25600
	v_add_f32_e32 v173, v230, v234
	v_smfmac_f32_16x16x64_f16 v[238:241], v[146:149], a[144:151], v210
	ds_read_b128 v[230:233], v217
	s_waitcnt lgkmcnt(5)
	v_smfmac_f32_16x16x64_f16 v[242:245], v[146:149], v[188:195], v210
	ds_read_b128 v[188:191], v199 offset:28672
	ds_read_b128 v[192:195], v199 offset:29696
	ds_read_b128 v[234:237], v217
	v_smfmac_f32_16x16x64_f16 v[238:241], v[150:153], a[176:183], v210
	s_waitcnt lgkmcnt(6)
	v_smfmac_f32_16x16x64_f16 v[242:245], v[150:153], v[222:229], v210
	ds_read_b128 v[222:225], v199 offset:2048
	ds_read_b128 v[226:229], v199 offset:3072
	v_smfmac_f32_16x16x64_f16 v[238:241], v[154:157], a[208:215], v210
	s_waitcnt lgkmcnt(6)
	v_smfmac_f32_16x16x64_f16 v[242:245], v[154:157], v[180:187], v210
	ds_read_b128 v[180:183], v199 offset:6144
	ds_read_b128 v[184:187], v199 offset:7168
	v_smfmac_f32_16x16x64_f16 v[238:241], v[158:161], a[240:247], v210
	s_waitcnt lgkmcnt(5)
	v_smfmac_f32_16x16x64_f16 v[242:245], v[158:161], v[188:195], v210
	ds_read_b128 v[188:191], v199 offset:10240
	ds_read_b128 v[192:195], v199 offset:11264
	v_smfmac_f32_16x16x64_f16 v[230:233], v[130:133], a[8:15], v210
	s_waitcnt lgkmcnt(6)
	v_smfmac_f32_16x16x64_f16 v[234:237], v[130:133], v[2:9], v210
	v_smfmac_f32_16x16x64_f16 v[230:233], v[134:137], a[32:39], v210
	v_fmac_f32_e32 v238, s40, v239
	v_smfmac_f32_16x16x64_f16 v[234:237], v[134:137], v[10:17], v210
	v_fmac_f32_e32 v242, s40, v243
	v_smfmac_f32_16x16x64_f16 v[230:233], v[138:141], a[72:79], v210
	v_fmac_f32_e32 v238, s41, v240
	v_smfmac_f32_16x16x64_f16 v[234:237], v[138:141], v[50:57], v210
	v_fmac_f32_e32 v242, s41, v244
	v_smfmac_f32_16x16x64_f16 v[230:233], v[142:145], a[104:111], v210
	s_nop 0
	v_permlane32_swap_b32_e32 v238, v242
	v_smfmac_f32_16x16x64_f16 v[234:237], v[142:145], v[26:33], v210
	v_add_f32_e32 v175, v238, v242
	v_smfmac_f32_16x16x64_f16 v[230:233], v[146:149], a[136:143], v210
	ds_read_b128 v[238:241], v217
	v_smfmac_f32_16x16x64_f16 v[234:237], v[146:149], v[82:89], v210
	ds_read_b128 v[242:245], v217
	v_smfmac_f32_16x16x64_f16 v[230:233], v[150:153], a[168:175], v210
	v_smfmac_f32_16x16x64_f16 v[234:237], v[150:153], v[66:73], v210
	v_smfmac_f32_16x16x64_f16 v[230:233], v[154:157], a[200:207], v210
	v_smfmac_f32_16x16x64_f16 v[234:237], v[154:157], v[114:121], v210
	v_smfmac_f32_16x16x64_f16 v[230:233], v[158:161], a[232:239], v210
	v_smfmac_f32_16x16x64_f16 v[234:237], v[158:161], v[90:97], v210
	s_waitcnt lgkmcnt(1)
	v_smfmac_f32_16x16x64_f16 v[238:241], v[130:133], a[24:31], v210
	s_waitcnt lgkmcnt(0)
	v_smfmac_f32_16x16x64_f16 v[242:245], v[130:133], v[222:229], v210
	ds_read_b128 v[222:225], v199 offset:14336
	ds_read_b128 v[226:229], v199 offset:15360
	v_smfmac_f32_16x16x64_f16 v[238:241], v[134:137], a[56:63], v210
	v_fmac_f32_e32 v230, s40, v231
	v_smfmac_f32_16x16x64_f16 v[242:245], v[134:137], v[180:187], v210
	ds_read_b128 v[180:183], v199 offset:18432
	ds_read_b128 v[184:187], v199 offset:19456
	v_fmac_f32_e32 v234, s40, v235
	v_smfmac_f32_16x16x64_f16 v[238:241], v[138:141], a[88:95], v210
	v_fmac_f32_e32 v230, s41, v232
	v_smfmac_f32_16x16x64_f16 v[242:245], v[138:141], v[188:195], v210
	ds_read_b128 v[188:191], v199 offset:22528
	ds_read_b128 v[192:195], v199 offset:23552
	v_fmac_f32_e32 v234, s41, v236
	v_smfmac_f32_16x16x64_f16 v[238:241], v[142:145], a[120:127], v210
	s_nop 0
	v_permlane32_swap_b32_e32 v230, v234
	s_waitcnt lgkmcnt(4)
	v_smfmac_f32_16x16x64_f16 v[242:245], v[142:145], v[222:229], v210
	ds_read_b128 v[222:225], v199 offset:26624
	ds_read_b128 v[226:229], v199 offset:27648
	v_add_f32_e32 v172, v230, v234
	v_smfmac_f32_16x16x64_f16 v[238:241], v[146:149], a[152:159], v210
	ds_read_b128 v[230:233], v217
	s_waitcnt lgkmcnt(5)
	v_smfmac_f32_16x16x64_f16 v[242:245], v[146:149], v[180:187], v210
	ds_read_b128 v[180:183], v199 offset:30720
	ds_read_b128 v[184:187], v199 offset:31744
	ds_read_b128 v[234:237], v217
	v_smfmac_f32_16x16x64_f16 v[238:241], v[150:153], a[184:191], v210
	s_waitcnt lgkmcnt(6)
	v_smfmac_f32_16x16x64_f16 v[242:245], v[150:153], v[188:195], v210
	v_smfmac_f32_16x16x64_f16 v[238:241], v[154:157], a[216:223], v210
	s_waitcnt lgkmcnt(4)
	v_smfmac_f32_16x16x64_f16 v[242:245], v[154:157], v[222:229], v210
	v_smfmac_f32_16x16x64_f16 v[238:241], v[158:161], a[248:255], v210
	s_waitcnt lgkmcnt(1)
	v_smfmac_f32_16x16x64_f16 v[242:245], v[158:161], v[180:187], v210
	s_nop 5
	v_fmac_f32_e32 v238, s40, v239
	s_nop 0
	v_fmac_f32_e32 v242, s40, v243
	v_fmac_f32_e32 v238, s41, v240
	v_fmac_f32_e32 v242, s41, v244
	s_nop 1
	v_permlane32_swap_b32_e32 v238, v242
	v_add_f32_e32 v174, v238, v242
	s_mov_b32 s52, 0x3a83126f
	v_mov_b32_e32 v245, 0x358637bd
	v_fma_f32 v179, |v171|, s52, v245
	v_fma_f32 v196, |v170|, s52, v245
	v_fma_f32 v197, |v169|, s52, v245
	v_fma_f32 v198, |v168|, s52, v245
	v_rcp_f32_e32 v179, v179
	v_rcp_f32_e32 v196, v196
	v_rcp_f32_e32 v197, v197
	v_rcp_f32_e32 v198, v198
	v_mul_f32_e32 v238, v170, v196
	v_mul_f32_e32 v239, 0x3b000000, v172
	v_mul_f32_e32 v239, v239, v196
	v_mul_f32_e32 v130, v238, v238
	v_mul_f32_e32 v131, v239, v239
	v_mul_f32_e32 v238, v171, v179
	v_mul_f32_e32 v239, 0x3b000000, v173
	v_mul_f32_e32 v239, v239, v179
	v_fmac_f32_e32 v130, v238, v238
	v_fmac_f32_e32 v131, v239, v239
	v_mul_f32_e32 v238, v169, v197
	v_mul_f32_e32 v239, 0x3b000000, v175
	v_mul_f32_e32 v239, v239, v197
	v_fmac_f32_e32 v130, v238, v238
	v_fmac_f32_e32 v131, v239, v239
	v_mul_f32_e32 v238, v168, v198
	v_mul_f32_e32 v239, 0x3b000000, v174
	v_mul_f32_e32 v239, v239, v198
	v_fmac_f32_e32 v130, v238, v238
	v_fmac_f32_e32 v131, v239, v239
	s_nop 0
	v_add_f32_dpp v130, v130, v130 quad_perm:[1,0,3,2] row_mask:0xf bank_mask:0xf bound_ctrl:1
	v_add_f32_dpp v131, v131, v131 quad_perm:[1,0,3,2] row_mask:0xf bank_mask:0xf bound_ctrl:1
	s_nop 0
	v_add_f32_dpp v130, v130, v130 quad_perm:[2,3,0,1] row_mask:0xf bank_mask:0xf bound_ctrl:1
	v_add_f32_dpp v131, v131, v131 quad_perm:[2,3,0,1] row_mask:0xf bank_mask:0xf bound_ctrl:1
	s_nop 0
	v_add_f32_dpp v130, v130, v130 row_half_mirror row_mask:0xf bank_mask:0xf bound_ctrl:1
	v_add_f32_dpp v131, v131, v131 row_half_mirror row_mask:0xf bank_mask:0xf bound_ctrl:1
	s_nop 0
	v_add_f32_dpp v130, v130, v130 row_mirror row_mask:0xf bank_mask:0xf bound_ctrl:1
	v_add_f32_dpp v131, v131, v131 row_mirror row_mask:0xf bank_mask:0xf bound_ctrl:1
	v_mov_b32_e32 v240, v130
	v_mov_b32_e32 v241, v131
	s_nop 0
	v_permlane32_swap_b32_e32 v130, v240
	v_permlane32_swap_b32_e32 v131, v241
	v_add_f32_e32 v130, v130, v240
	v_add_f32_e32 v131, v131, v241
	v_add_u32_e32 v242, 0, v218
	v_lshlrev_b32_e32 v243, 3, v201
	v_or_b32_e32 v243, 0x24400, v243
	s_and_saveexec_b64 s[2:3], s[4:5]
	ds_write_b64 v242, v[130:131]
	s_or_b64 exec, exec, s[2:3]
	s_waitcnt lgkmcnt(0)
	s_barrier
	ds_read_b64 v[134:135], v243 offset:0
	ds_read_b64 v[138:139], v243 offset:16
	ds_read_b64 v[142:143], v243 offset:32
	ds_read_b64 v[146:147], v243 offset:48
	s_waitcnt lgkmcnt(2)
	v_add_f32_e32 v238, v134, v138
	s_waitcnt lgkmcnt(1)
	v_add_f32_e32 v238, v238, v142
	s_waitcnt lgkmcnt(0)
	v_add_f32_e32 v238, v238, v146
	v_add_f32_e32 v239, v135, v139
	v_add_f32_e32 v239, v239, v143
	v_add_f32_e32 v239, v239, v147
	v_mul_f32_e32 v238, 0x3b000000, v238
	v_max_f32_e32 v238, 0xda24260, v238
	v_sqrt_f32_e32 v238, v238
	v_mul_f32_e32 v239, 0x3b000000, v239
	v_max_f32_e32 v239, 0xda24260, v239
	v_sqrt_f32_e32 v239, v239
	s_nop 0
	v_mov_b32_e32 v220, v239
	v_rcp_f32_e32 v240, v239
	v_min_f32_e32 v241, v238, v239
	v_mul_f32_e32 v238, 0x3c23d70a, v238
	v_mul_f32_e32 v238, v238, v240
	s_mov_b32 s52, 0x3727c5ac
	v_cmp_ngt_f32_e32 vcc, s52, v241
	v_mov_b32_e32 v240, 0x358637bd
	s_nop 1
	v_cndmask_b32_e32 v219, v240, v238, vcc
	v_mul_f32_e32 v178, 0x3b000000, v219
	v_fma_mixlo_f16 v131, v178, v173, v171
	v_fma_mixlo_f16 v139, v178, v172, v170
	v_fma_mixlo_f16 v147, v178, v175, v169
	v_fma_mixlo_f16 v155, v178, v174, v168
	v_fma_f32 v130, v178, v173, v171
	v_fma_f32 v138, v178, v172, v170
	v_fma_f32 v146, v178, v175, v169
	v_fma_f32 v154, v178, v174, v168
	v_fma_mix_f32 v130, v130, 1.0, -v131 op_sel_hi:[0,0,1]
	v_fma_mix_f32 v138, v138, 1.0, -v139 op_sel_hi:[0,0,1]
	v_fma_mix_f32 v146, v146, 1.0, -v147 op_sel_hi:[0,0,1]
	v_fma_mix_f32 v154, v154, 1.0, -v155 op_sel_hi:[0,0,1]
	v_fma_mixlo_f16 v133, v130, s42, 0
	v_fma_mixlo_f16 v141, v138, s42, 0
	v_fma_mixlo_f16 v149, v146, s42, 0
	v_fma_mixlo_f16 v157, v154, s42, 0
	v_fma_mix_f32 v130, v130, s42, -v133 op_sel_hi:[0,0,1]
	v_fma_mix_f32 v138, v138, s42, -v141 op_sel_hi:[0,0,1]
	v_fma_mix_f32 v146, v146, s42, -v149 op_sel_hi:[0,0,1]
	v_fma_mix_f32 v154, v154, s42, -v157 op_sel_hi:[0,0,1]
	v_fma_mixlo_f16 v132, v130, s42, 0
	v_fma_mixlo_f16 v140, v138, s42, 0
	v_fma_mixlo_f16 v148, v146, s42, 0
	v_fma_mixlo_f16 v156, v154, s42, 0
	ds_write_b16 v204, v131 offset:8704
	ds_write_b16 v205, v139 offset:8704
	ds_write_b16 v206, v147 offset:8704
	ds_write_b16 v207, v155 offset:8704
	ds_write_b16 v204, v133 offset:9248
	ds_write_b16 v205, v141 offset:9248
	ds_write_b16 v206, v149 offset:9248
	ds_write_b16 v207, v157 offset:9248
	ds_write_b16 v204, v132 offset:9792
	ds_write_b16 v205, v140 offset:9792
	ds_write_b16 v206, v148 offset:9792
	ds_write_b16 v207, v156 offset:9792
	s_waitcnt lgkmcnt(0)
	s_barrier
	ds_read_b128 v[130:133], v208 offset:8704
	ds_read_b128 v[134:137], v209 offset:8768
	ds_read_b128 v[138:141], v211 offset:8704
	ds_read_b128 v[142:145], v212 offset:8704
	ds_read_b128 v[146:149], v213 offset:8704
	ds_read_b128 v[150:153], v214 offset:8704
	ds_read_b128 v[154:157], v215 offset:8704
	ds_read_b128 v[158:161], v216 offset:8704
	ds_read_b128 v[180:183], v199 offset:0
	ds_read_b128 v[184:187], v199 offset:1024
	ds_read_b128 v[188:191], v199 offset:4096
	ds_read_b128 v[192:195], v199 offset:5120
	ds_read_b128 v[222:225], v199 offset:8192
	s_waitcnt lgkmcnt(6)
	ds_read_b128 v[226:229], v199 offset:9216
	v_smfmac_f32_16x16x64_f16 v[230:233], v[130:133], a[0:7], v210
	ds_read_b128 v[238:241], v217
	v_smfmac_f32_16x16x64_f16 v[234:237], v[130:133], v[18:25], v210
	ds_read_b128 v[242:245], v217
	v_smfmac_f32_16x16x64_f16 v[230:233], v[134:137], a[40:47], v210
	v_smfmac_f32_16x16x64_f16 v[234:237], v[134:137], v[34:41], v210
	v_smfmac_f32_16x16x64_f16 v[230:233], v[138:141], a[64:71], v210
	v_smfmac_f32_16x16x64_f16 v[234:237], v[138:141], v[42:49], v210
	v_smfmac_f32_16x16x64_f16 v[230:233], v[142:145], a[96:103], v210
	v_smfmac_f32_16x16x64_f16 v[234:237], v[142:145], v[58:65], v210
	v_smfmac_f32_16x16x64_f16 v[230:233], v[146:149], a[128:135], v210
	v_smfmac_f32_16x16x64_f16 v[234:237], v[146:149], v[74:81], v210
	v_smfmac_f32_16x16x64_f16 v[230:233], v[150:153], a[160:167], v210
	v_smfmac_f32_16x16x64_f16 v[234:237], v[150:153], v[98:105], v210
	v_smfmac_f32_16x16x64_f16 v[230:233], v[154:157], a[192:199], v210
	v_smfmac_f32_16x16x64_f16 v[234:237], v[154:157], v[106:113], v210
	s_waitcnt lgkmcnt(8)
	v_smfmac_f32_16x16x64_f16 v[230:233], v[158:161], a[224:231], v210
	v_smfmac_f32_16x16x64_f16 v[234:237], v[158:161], v[122:129], v210
	s_waitcnt lgkmcnt(1)
	v_smfmac_f32_16x16x64_f16 v[238:241], v[130:133], a[16:23], v210
	s_waitcnt lgkmcnt(0)
	v_smfmac_f32_16x16x64_f16 v[242:245], v[130:133], v[180:187], v210
	ds_read_b128 v[180:183], v199 offset:12288
	ds_read_b128 v[184:187], v199 offset:13312
	v_smfmac_f32_16x16x64_f16 v[238:241], v[134:137], a[48:55], v210
	v_fmac_f32_e32 v230, s40, v231
	v_smfmac_f32_16x16x64_f16 v[242:245], v[134:137], v[188:195], v210
	ds_read_b128 v[188:191], v199 offset:16384
	ds_read_b128 v[192:195], v199 offset:17408
	v_fmac_f32_e32 v234, s40, v235
	v_smfmac_f32_16x16x64_f16 v[238:241], v[138:141], a[80:87], v210
	v_fmac_f32_e32 v230, s41, v232
	v_smfmac_f32_16x16x64_f16 v[242:245], v[138:141], v[222:229], v210
	ds_read_b128 v[222:225], v199 offset:20480
	ds_read_b128 v[226:229], v199 offset:21504
	v_fmac_f32_e32 v234, s41, v236
	v_smfmac_f32_16x16x64_f16 v[238:241], v[142:145], a[112:119], v210
	s_nop 0
	v_permlane32_swap_b32_e32 v230, v234
	s_waitcnt lgkmcnt(4)
	v_smfmac_f32_16x16x64_f16 v[242:245], v[142:145], v[180:187], v210
	ds_read_b128 v[180:183], v199 offset:24576
	ds_read_b128 v[184:187], v199 offset:25600
	v_add_f32_e32 v162, v230, v234
	v_smfmac_f32_16x16x64_f16 v[238:241], v[146:149], a[144:151], v210
	ds_read_b128 v[230:233], v217
	s_waitcnt lgkmcnt(5)
	v_smfmac_f32_16x16x64_f16 v[242:245], v[146:149], v[188:195], v210
	ds_read_b128 v[188:191], v199 offset:28672
	ds_read_b128 v[192:195], v199 offset:29696
	ds_read_b128 v[234:237], v217
	v_smfmac_f32_16x16x64_f16 v[238:241], v[150:153], a[176:183], v210
	s_waitcnt lgkmcnt(6)
	v_smfmac_f32_16x16x64_f16 v[242:245], v[150:153], v[222:229], v210
	ds_read_b128 v[222:225], v199 offset:2048
	ds_read_b128 v[226:229], v199 offset:3072
	v_smfmac_f32_16x16x64_f16 v[238:241], v[154:157], a[208:215], v210
	s_waitcnt lgkmcnt(6)
	v_smfmac_f32_16x16x64_f16 v[242:245], v[154:157], v[180:187], v210
	ds_read_b128 v[180:183], v199 offset:6144
	ds_read_b128 v[184:187], v199 offset:7168
	v_smfmac_f32_16x16x64_f16 v[238:241], v[158:161], a[240:247], v210
	s_waitcnt lgkmcnt(5)
	v_smfmac_f32_16x16x64_f16 v[242:245], v[158:161], v[188:195], v210
	ds_read_b128 v[188:191], v199 offset:10240
	ds_read_b128 v[192:195], v199 offset:11264
	v_smfmac_f32_16x16x64_f16 v[230:233], v[130:133], a[8:15], v210
	s_waitcnt lgkmcnt(6)
	v_smfmac_f32_16x16x64_f16 v[234:237], v[130:133], v[2:9], v210
	v_smfmac_f32_16x16x64_f16 v[230:233], v[134:137], a[32:39], v210
	v_fmac_f32_e32 v238, s40, v239
	v_smfmac_f32_16x16x64_f16 v[234:237], v[134:137], v[10:17], v210
	v_fmac_f32_e32 v242, s40, v243
	v_smfmac_f32_16x16x64_f16 v[230:233], v[138:141], a[72:79], v210
	v_fmac_f32_e32 v238, s41, v240
	v_smfmac_f32_16x16x64_f16 v[234:237], v[138:141], v[50:57], v210
	v_fmac_f32_e32 v242, s41, v244
	v_smfmac_f32_16x16x64_f16 v[230:233], v[142:145], a[104:111], v210
	s_nop 0
	v_permlane32_swap_b32_e32 v238, v242
	v_smfmac_f32_16x16x64_f16 v[234:237], v[142:145], v[26:33], v210
	v_add_f32_e32 v164, v238, v242
	v_smfmac_f32_16x16x64_f16 v[230:233], v[146:149], a[136:143], v210
	ds_read_b128 v[238:241], v217
	v_smfmac_f32_16x16x64_f16 v[234:237], v[146:149], v[82:89], v210
	ds_read_b128 v[242:245], v217
	v_smfmac_f32_16x16x64_f16 v[230:233], v[150:153], a[168:175], v210
	v_smfmac_f32_16x16x64_f16 v[234:237], v[150:153], v[66:73], v210
	v_smfmac_f32_16x16x64_f16 v[230:233], v[154:157], a[200:207], v210
	v_smfmac_f32_16x16x64_f16 v[234:237], v[154:157], v[114:121], v210
	v_smfmac_f32_16x16x64_f16 v[230:233], v[158:161], a[232:239], v210
	v_smfmac_f32_16x16x64_f16 v[234:237], v[158:161], v[90:97], v210
	s_waitcnt lgkmcnt(1)
	v_smfmac_f32_16x16x64_f16 v[238:241], v[130:133], a[24:31], v210
	s_waitcnt lgkmcnt(0)
	v_smfmac_f32_16x16x64_f16 v[242:245], v[130:133], v[222:229], v210
	ds_read_b128 v[222:225], v199 offset:14336
	ds_read_b128 v[226:229], v199 offset:15360
	v_smfmac_f32_16x16x64_f16 v[238:241], v[134:137], a[56:63], v210
	v_fmac_f32_e32 v230, s40, v231
	v_smfmac_f32_16x16x64_f16 v[242:245], v[134:137], v[180:187], v210
	ds_read_b128 v[180:183], v199 offset:18432
	ds_read_b128 v[184:187], v199 offset:19456
	v_fmac_f32_e32 v234, s40, v235
	v_smfmac_f32_16x16x64_f16 v[238:241], v[138:141], a[88:95], v210
	v_fmac_f32_e32 v230, s41, v232
	v_smfmac_f32_16x16x64_f16 v[242:245], v[138:141], v[188:195], v210
	ds_read_b128 v[188:191], v199 offset:22528
	ds_read_b128 v[192:195], v199 offset:23552
	v_fmac_f32_e32 v234, s41, v236
	v_smfmac_f32_16x16x64_f16 v[238:241], v[142:145], a[120:127], v210
	s_nop 0
	v_permlane32_swap_b32_e32 v230, v234
	s_waitcnt lgkmcnt(4)
	v_smfmac_f32_16x16x64_f16 v[242:245], v[142:145], v[222:229], v210
	ds_read_b128 v[222:225], v199 offset:26624
	ds_read_b128 v[226:229], v199 offset:27648
	v_add_f32_e32 v163, v230, v234
	v_smfmac_f32_16x16x64_f16 v[238:241], v[146:149], a[152:159], v210
	ds_read_b128 v[230:233], v217
	s_waitcnt lgkmcnt(5)
	v_smfmac_f32_16x16x64_f16 v[242:245], v[146:149], v[180:187], v210
	ds_read_b128 v[180:183], v199 offset:30720
	ds_read_b128 v[184:187], v199 offset:31744
	ds_read_b128 v[234:237], v217
	v_smfmac_f32_16x16x64_f16 v[238:241], v[150:153], a[184:191], v210
	s_waitcnt lgkmcnt(6)
	v_smfmac_f32_16x16x64_f16 v[242:245], v[150:153], v[188:195], v210
	v_smfmac_f32_16x16x64_f16 v[238:241], v[154:157], a[216:223], v210
	s_waitcnt lgkmcnt(4)
	v_smfmac_f32_16x16x64_f16 v[242:245], v[154:157], v[222:229], v210
	v_smfmac_f32_16x16x64_f16 v[238:241], v[158:161], a[248:255], v210
	s_waitcnt lgkmcnt(1)
	v_smfmac_f32_16x16x64_f16 v[242:245], v[158:161], v[180:187], v210
	s_nop 5
	v_fmac_f32_e32 v238, s40, v239
	s_nop 0
	v_fmac_f32_e32 v242, s40, v243
	v_fmac_f32_e32 v238, s41, v240
	v_fmac_f32_e32 v242, s41, v244
	s_nop 1
	v_permlane32_swap_b32_e32 v238, v242
	v_add_f32_e32 v165, v238, v242
	v_sub_f32_e32 v238, v163, v172
	v_mul_f32_e32 v238, 0x3b000000, v238
	v_mul_f32_e32 v238, v238, v196
	v_mul_f32_e32 v130, v238, v238
	v_sub_f32_e32 v238, v162, v173
	v_mul_f32_e32 v238, 0x3b000000, v238
	v_mul_f32_e32 v238, v238, v179
	v_fmac_f32_e32 v130, v238, v238
	v_sub_f32_e32 v238, v164, v175
	v_mul_f32_e32 v238, 0x3b000000, v238
	v_mul_f32_e32 v238, v238, v197
	v_fmac_f32_e32 v130, v238, v238
	v_sub_f32_e32 v238, v165, v174
	v_mul_f32_e32 v238, 0x3b000000, v238
	v_mul_f32_e32 v238, v238, v198
	v_fmac_f32_e32 v130, v238, v238
	s_nop 1
	v_add_f32_dpp v130, v130, v130 quad_perm:[1,0,3,2] row_mask:0xf bank_mask:0xf bound_ctrl:1
	s_nop 1
	v_add_f32_dpp v130, v130, v130 quad_perm:[2,3,0,1] row_mask:0xf bank_mask:0xf bound_ctrl:1
	s_nop 1
	v_add_f32_dpp v130, v130, v130 row_half_mirror row_mask:0xf bank_mask:0xf bound_ctrl:1
	s_nop 1
	v_add_f32_dpp v130, v130, v130 row_mirror row_mask:0xf bank_mask:0xf bound_ctrl:1
	v_mov_b32_e32 v240, v130
	s_nop 1
	v_permlane32_swap_b32_e32 v130, v240
	v_add_f32_e32 v130, v130, v240
	v_add_u32_e32 v242, 64, v218
	v_lshlrev_b32_e32 v243, 3, v201
	v_or_b32_e32 v243, 0x24440, v243
	s_and_saveexec_b64 s[2:3], s[4:5]
	ds_write_b32 v242, v130
	s_or_b64 exec, exec, s[2:3]
	s_waitcnt lgkmcnt(0)
	s_barrier
	ds_read2_b32 v[134:135], v243 offset1:4
	ds_read2_b32 v[136:137], v243 offset0:8 offset1:12
	s_waitcnt lgkmcnt(1)
	v_add_f32_e32 v238, v134, v135
	s_waitcnt lgkmcnt(0)
	v_add_f32_e32 v238, v238, v136
	v_add_f32_e32 v238, v238, v137
	v_mul_f32_e32 v238, 0x3b000000, v238
	v_max_f32_e32 v238, 0xda24260, v238
	v_rcp_f32_e32 v240, v219
	v_sqrt_f32_e32 v238, v238
	s_nop 0
	v_mul_f32_e32 v238, v240, v238
	v_max_f32_e32 v241, v220, v238
	v_mul_f32_e32 v242, 0x3a83126f, v219
	v_max_f32_e32 v242, 0x358637bd, v242
	v_max_f32_e32 v243, 0x26901d7d, v241
	v_rcp_f32_e32 v243, v243
	s_nop 0
	v_mul_f32_e32 v243, 0x3c23d70a, v243
	v_log_f32_e32 v243, v243
	s_nop 0
	v_mul_f32_e32 v243, 0x3e4ccccd, v243
	v_exp_f32_e32 v243, v243
	s_mov_b32 s52, 0x26901d7d
	v_cmp_ge_f32_e32 vcc, s52, v241
	s_nop 1
	v_cndmask_b32_e32 v243, v243, v242, vcc
	v_mul_f32_e32 v242, 0x42c80000, v219
	v_min3_f32 v1, v242, v243, 1.0

amdhsa.kernels:
  - .agpr_count:     0
    .args:
      - .actual_access:  read_only
        .address_space:  global
        .offset:         0
        .size:           8
        .value_kind:     global_buffer
      - .actual_access:  read_only
        .address_space:  global
        .offset:         8
        .size:           8
        .value_kind:     global_buffer
      - .actual_access:  read_only
        .address_space:  global
        .offset:         16
        .size:           8
        .value_kind:     global_buffer
      - .actual_access:  write_only
        .address_space:  global
        .offset:         24
        .size:           8
        .value_kind:     global_buffer
      - .actual_access:  write_only
        .address_space:  global
        .offset:         32
        .size:           8
        .value_kind:     global_buffer
      - .actual_access:  write_only
        .address_space:  global
        .offset:         40
        .size:           8
        .value_kind:     global_buffer
      - .actual_access:  read_only
        .address_space:  global
        .offset:         48
        .size:           8
        .value_kind:     global_buffer
      - .actual_access:  write_only
        .address_space:  global
        .offset:         56
        .size:           8
        .value_kind:     global_buffer
    .group_segment_fixed_size: 24576
    .kernarg_segment_align: 8
    .kernarg_segment_size: 64
    .language:       OpenCL C
    .language_version:
      - 2
      - 0
    .max_flat_workgroup_size: 512
    .name:           _Z11prep_kernelPKfS0_S0_PDF16_PfPiS0_S1_
    .private_segment_fixed_size: 0
    .sgpr_count:     90
    .sgpr_spill_count: 0
    .symbol:         _Z11prep_kernelPKfS0_S0_PDF16_PfPiS0_S1_.kd
    .uniform_work_group_size: 1
    .uses_dynamic_stack: false
    .vgpr_count:     66
    .vgpr_spill_count: 0
    .wavefront_size: 64
  - .agpr_count:     256
    .args:
      - .actual_access:  read_only
        .address_space:  global
        .offset:         0
        .size:           8
        .value_kind:     global_buffer
      - .actual_access:  read_only
        .address_space:  global
        .offset:         8
        .size:           8
        .value_kind:     global_buffer
      - .actual_access:  read_only
        .address_space:  global
        .offset:         16
        .size:           8
        .value_kind:     global_buffer
      - .actual_access:  write_only
        .address_space:  global
        .offset:         24
        .size:           8
        .value_kind:     global_buffer
      - .actual_access:  read_only
        .address_space:  global
        .offset:         32
        .size:           8
        .value_kind:     global_buffer
    .group_segment_fixed_size: 148624
    .kernarg_segment_align: 8
    .kernarg_segment_size: 40
    .language:       OpenCL C
    .language_version:
      - 2
      - 0
    .max_flat_workgroup_size: 256
    .name:           _Z10ode_kernelPKfPKDF16_S2_PfPKi
    .private_segment_fixed_size: 0
    .sgpr_count:     59
    .sgpr_spill_count: 0
    .symbol:         _Z10ode_kernelPKfPKDF16_S2_PfPKi.kd
    .uniform_work_group_size: 1
    .uses_dynamic_stack: false
    .vgpr_count:     512
    .vgpr_spill_count: 0
    .wavefront_size: 64
